# speedup vs baseline: 1.1217x; 1.0147x over previous
.Lpp_z2:
	v_xor_b32_e32 v59, 16, v58
	v_lshlrev_b32_e32 v59, 2, v59
	v_xor_b32_e32 v61, 32, v58
	v_lshlrev_b32_e32 v61, 2, v61
	s_mul_i32 s3, s15, 0x900
	v_mul_u32_u24_e32 v57, 0x90, v62
	v_lshl_add_u32 v57, v63, 4, v57
	v_add_u32_e32 v57, s3, v57
	v_mul_u32_u24_e32 v56, 0x480, v62
	v_mul_u32_u24_e32 v55, 0x90, v63
	v_add3_u32 v56, v56, v55, s3
	s_lshl_b32 s6, s15, 1
	v_lshrrev_b32_e32 v55, 1, v63
	v_and_b32_e32 v54, 1, v63
	v_lshlrev_b32_e32 v55, 10, v55
	v_lshl_or_b32 v55, v54, 9, v55
	v_add_u32_e32 v54, s6, v62
	v_lshl_or_b32 v55, v54, 4, v55
	v_mov_b32_e32 v52, 1.0
	s_mul_i32 s6, s8, 0x1800
	s_add_u32 s10, s22, s6
	s_addc_u32 s11, s23, 0
	s_waitcnt vmcnt(1)
	v_pk_mul_f32 v[10:11], v[2:3], v[2:3]
	v_pk_fma_f32 v[10:11], v[4:5], v[4:5], v[10:11]
	s_waitcnt vmcnt(0)
	v_pk_mul_f32 v[12:13], v[6:7], v[6:7]
	v_pk_fma_f32 v[12:13], v[8:9], v[8:9], v[12:13]
	v_add_f32_e32 v10, v10, v11
	v_add_f32_e32 v12, v12, v13
	s_nop 1
	v_add_f32_dpp v10, v10, v10 quad_perm:[1,0,3,2] row_mask:0xf bank_mask:0xf bound_ctrl:1
	v_add_f32_dpp v12, v12, v12 quad_perm:[1,0,3,2] row_mask:0xf bank_mask:0xf bound_ctrl:1
	s_nop 1
	v_add_f32_dpp v10, v10, v10 quad_perm:[2,3,0,1] row_mask:0xf bank_mask:0xf bound_ctrl:1
	v_add_f32_dpp v12, v12, v12 quad_perm:[2,3,0,1] row_mask:0xf bank_mask:0xf bound_ctrl:1
	s_nop 1
	v_add_f32_dpp v10, v10, v10 row_half_mirror row_mask:0xf bank_mask:0xf bound_ctrl:1
	v_add_f32_dpp v12, v12, v12 row_half_mirror row_mask:0xf bank_mask:0xf bound_ctrl:1
	s_nop 1
	v_add_f32_dpp v10, v10, v10 row_mirror row_mask:0xf bank_mask:0xf bound_ctrl:1
	v_add_f32_dpp v12, v12, v12 row_mirror row_mask:0xf bank_mask:0xf bound_ctrl:1
	ds_bpermute_b32 v11, v59, v10
	ds_bpermute_b32 v13, v59, v12
	s_waitcnt lgkmcnt(1)
	v_add_f32_e32 v10, v10, v11
	s_waitcnt lgkmcnt(0)
	v_add_f32_e32 v12, v12, v13
	ds_bpermute_b32 v11, v61, v10
	ds_bpermute_b32 v13, v61, v12
	s_waitcnt lgkmcnt(1)
	v_add_f32_e32 v10, v10, v11
	s_waitcnt lgkmcnt(0)
	v_add_f32_e32 v12, v12, v13
	v_rsq_f32_e32 v10, v10
	v_rsq_f32_e32 v12, v12
	s_nop 0
	v_min_f32_e32 v10, 0x4cbebc20, v10
	v_min_f32_e32 v12, 0x4cbebc20, v12
	v_mul_f32_e32 v10, s14, v10
	v_mul_f32_e32 v12, s14, v12
	v_pk_mul_f32 v[2:3], v[2:3], v[10:11] op_sel_hi:[1,0]
	v_pk_mul_f32 v[4:5], v[4:5], v[10:11] op_sel_hi:[1,0]
	v_pk_mul_f32 v[6:7], v[6:7], v[12:13] op_sel_hi:[1,0]
	v_pk_mul_f32 v[8:9], v[8:9], v[12:13] op_sel_hi:[1,0]
	ds_write_b128 v57, v[2:5]
	ds_write_b128 v57, v[6:9] offset:1152
	s_nop 1
	v_pk_add_f32 v[2:3], v[2:3], v[6:7]
	v_pk_add_f32 v[4:5], v[4:5], v[8:9]
	s_mov_b64 exec, 0xffff
	ds_read_b128 v[12:15], v56
	ds_read_b128 v[16:19], v56 offset:16
	ds_read_b128 v[20:23], v56 offset:32
	ds_read_b128 v[24:27], v56 offset:48
	ds_read_b128 v[28:31], v56 offset:64
	ds_read_b128 v[32:35], v56 offset:80
	ds_read_b128 v[36:39], v56 offset:96
	ds_read_b128 v[40:43], v56 offset:112
	v_mov_b32_e32 v50, 0
	v_mov_b32_e32 v51, 0
	s_waitcnt lgkmcnt(0)
	v_cvt_scalef32_2xpk16_fp6_f32 v[44:49], v[12:27], v[28:43], v52
	s_nop 1
	v_lshrrev_b32_e32 v54, 1, v55
	v_or_b32_e32 v54, 0x1000, v54
	global_store_dwordx4 v55, v[44:47], s[10:11]
	global_store_dwordx2 v54, v[48:49], s[10:11]
	s_mov_b64 exec, -1
	s_cmp_lt_u32 s8, 0x100
	s_cbranch_scc0 .Lpp_end
	v_add_u32_e32 v10, s3, v60
	ds_write_b128 v10, v[2:5]
	s_waitcnt lgkmcnt(0)
	s_barrier
	s_sub_u32 s6, s15, 8
	s_cmp_gt_u32 s6, 3
	s_cbranch_scc1 .Lpp_end
	s_lshl_b32 s6, s6, 8
	v_lshl_add_u32 v10, v58, 2, s6
	ds_read_b32 v12, v10
	ds_read_b32 v13, v10 offset:2304
	ds_read_b32 v14, v10 offset:4608
	ds_read_b32 v15, v10 offset:6912
	ds_read_b32 v16, v10 offset:9216
	ds_read_b32 v17, v10 offset:11520
	ds_read_b32 v18, v10 offset:13824
	ds_read_b32 v19, v10 offset:16128
	ds_read_b32 v20, v10 offset:18432
	ds_read_b32 v21, v10 offset:20736
	ds_read_b32 v22, v10 offset:23040
	ds_read_b32 v23, v10 offset:25344
	ds_read_b32 v24, v10 offset:27648
	ds_read_b32 v25, v10 offset:29952
	ds_read_b32 v26, v10 offset:32256
	ds_read_b32 v27, v10 offset:34560
	s_cmp_lt_u32 s8, 0x80
	s_cselect_b32 s10, s24, s26
	s_cselect_b32 s11, s25, s27
	s_and_b32 s6, s8, 0x7f
	s_lshl_b32 s6, s6, 10
	s_add_u32 s10, s10, s6
	s_addc_u32 s11, s11, 0
	s_waitcnt lgkmcnt(14)
	v_add_f32_e32 v12, v12, v13
	s_waitcnt lgkmcnt(13)
	v_add_f32_e32 v12, v12, v14
	s_waitcnt lgkmcnt(12)
	v_add_f32_e32 v12, v12, v15
	s_waitcnt lgkmcnt(11)
	v_add_f32_e32 v12, v12, v16
	s_waitcnt lgkmcnt(10)
	v_add_f32_e32 v12, v12, v17
	s_waitcnt lgkmcnt(9)
	v_add_f32_e32 v12, v12, v18
	s_waitcnt lgkmcnt(8)
	v_add_f32_e32 v12, v12, v19
	s_waitcnt lgkmcnt(7)
	v_add_f32_e32 v12, v12, v20
	s_waitcnt lgkmcnt(6)
	v_add_f32_e32 v12, v12, v21
	s_waitcnt lgkmcnt(5)
	v_add_f32_e32 v12, v12, v22
	s_waitcnt lgkmcnt(4)
	v_add_f32_e32 v12, v12, v23
	s_waitcnt lgkmcnt(3)
	v_add_f32_e32 v12, v12, v24
	s_waitcnt lgkmcnt(2)
	v_add_f32_e32 v12, v12, v25
	s_waitcnt lgkmcnt(1)
	v_add_f32_e32 v12, v12, v26
	s_waitcnt lgkmcnt(0)
	v_add_f32_e32 v12, v12, v27
	global_store_dword v10, v12, s[10:11]

.Lmk_start:
	s_mov_b32 s28, s8
	s_mov_b64 s[30:31], s[4:5]
	s_mov_b64 s[32:33], s[6:7]
	s_mov_b64 s[6:7], s[2:3]
	s_mov_b32 s2, s28
	s_and_b32 s3, s2, 7
	s_lshr_b32 s4, s2, 3
	s_and_b32 s5, s4, 3
	s_lshl_b32 s3, s3, 2
	s_or_b32 s8, s3, s5
	s_lshr_b32 s9, s4, 2
	v_lshrrev_b32_e32 v127, 6, v0
	v_and_b32_e32 v124, 63, v0
	v_lshlrev_b32_e32 v125, 3, v124
	v_lshlrev_b32_e32 v124, 4, v124
	v_readfirstlane_b32 s12, v127
	v_mov_b32_e32 v120, 0
	v_mov_b32_e32 v121, 0
	v_mov_b32_e32 v122, 0
	v_mov_b32_e32 v123, 0
	s_lshl_b32 s13, s12, 10
	s_lshl_b32 s14, s9, 3
	s_add_u32 s14, s14, s12
	s_mul_i32 s15, s14, 0x1800
	s_mul_i32 s16, s8, 0x12000
	s_add_u32 s16, s16, 0xc0000
	s_add_u32 s16, s16, s13
	s_add_u32 s20, s13, 0x2000
	s_add_u32 s10, s6, s16
	s_addc_u32 s11, s7, 0
	s_add_u32 s18, s6, s15
	s_addc_u32 s19, s7, 0
	s_add_u32 s22, s18, 0x1000
	s_addc_u32 s23, s19, 0
	s_cmp_lt_u32 s12, 4
	s_cbranch_scc0 .Lmk_vb
	s_mov_b32 m0, s13
	s_nop 0
	global_load_lds_dwordx4 v124, s[10:11]
	s_add_u32 s26, s10, 0x2000
	s_addc_u32 s27, s11, 0
	s_mov_b32 m0, s20
	s_nop 0
	global_load_lds_dwordx4 v124, s[26:27]
	global_load_dwordx4 v[96:99], v124, s[18:19]
	global_load_dwordx2 v[100:101], v125, s[22:23]
	global_load_dwordx4 v[102:105], v124, s[18:19] offset:1024
	global_load_dwordx2 v[106:107], v125, s[22:23] offset:512
	global_load_dwordx4 v[108:111], v124, s[18:19] offset:2048
	global_load_dwordx2 v[112:113], v125, s[22:23] offset:1024
	global_load_dwordx4 v[114:117], v124, s[18:19] offset:3072
	global_load_dwordx2 v[118:119], v125, s[22:23] offset:1536
	s_add_u32 s24, s10, 0x3000
	s_addc_u32 s25, s11, 0
	s_add_u32 s26, s13, 0x3000
	s_mov_b32 m0, s26
	s_nop 0
	global_load_lds_dwordx4 v124, s[24:25]
	s_add_u32 s26, s24, 0x2000
	s_addc_u32 s27, s25, 0
	s_add_u32 s29, s20, 0x3000
	s_mov_b32 m0, s29
	s_nop 0
	global_load_lds_dwordx4 v124, s[26:27]
	s_add_u32 s24, s10, 0x6000
	s_addc_u32 s25, s11, 0
	s_add_u32 s26, s13, 0x6000
	s_mov_b32 m0, s26
	s_nop 0
	global_load_lds_dwordx4 v124, s[24:25]
	s_add_u32 s26, s24, 0x2000
	s_addc_u32 s27, s25, 0
	s_add_u32 s29, s20, 0x6000
	s_mov_b32 m0, s29
	s_nop 0
	global_load_lds_dwordx4 v124, s[26:27]
	s_add_u32 s24, s10, 0x9000
	s_addc_u32 s25, s11, 0
	s_add_u32 s26, s13, 0x9000
	s_mov_b32 m0, s26
	s_nop 0
	global_load_lds_dwordx4 v124, s[24:25]
	s_add_u32 s26, s24, 0x2000
	s_addc_u32 s27, s25, 0
	s_add_u32 s29, s20, 0x9000
	s_mov_b32 m0, s29
	s_nop 0
	global_load_lds_dwordx4 v124, s[26:27]
	s_add_u32 s24, s10, 0xc000
	s_addc_u32 s25, s11, 0
	s_add_u32 s26, s13, 0xc000
	s_mov_b32 m0, s26
	s_nop 0
	global_load_lds_dwordx4 v124, s[24:25]
	s_add_u32 s26, s24, 0x2000
	s_addc_u32 s27, s25, 0
	s_add_u32 s29, s20, 0xc000
	s_mov_b32 m0, s29
	s_nop 0
	global_load_lds_dwordx4 v124, s[26:27]
	s_waitcnt vmcnt(8)
	s_barrier
	ds_read_b128 v[0:3], v124
	ds_read_b64 v[4:5], v125 offset:4096
	ds_read_b128 v[6:9], v124 offset:1024
	ds_read_b64 v[10:11], v125 offset:4608
	ds_read_b128 v[12:15], v124 offset:2048
	ds_read_b64 v[16:17], v125 offset:5120
	ds_read_b128 v[18:21], v124 offset:3072
	ds_read_b64 v[22:23], v125 offset:5632
	s_waitcnt lgkmcnt(0)
	s_setprio 3
	v_mfma_f32_32x32x64_f8f6f4 v[48:63], v[0:5], v[96:101], 0 cbsz:2 blgp:2
	ds_read_b128 v[24:27], v124 offset:6144
	ds_read_b64 v[28:29], v125 offset:10240
	v_mfma_f32_32x32x64_f8f6f4 v[48:63], v[6:11], v[102:107], v[48:63] cbsz:2 blgp:2
	ds_read_b128 v[30:33], v124 offset:7168
	ds_read_b64 v[34:35], v125 offset:10752
	v_mfma_f32_32x32x64_f8f6f4 v[48:63], v[12:17], v[108:113], v[48:63] cbsz:2 blgp:2
	ds_read_b128 v[36:39], v124 offset:8192
	ds_read_b64 v[40:41], v125 offset:11264
	v_mfma_f32_32x32x64_f8f6f4 v[48:63], v[18:23], v[114:119], v[48:63] cbsz:2 blgp:2
	ds_read_b128 v[42:45], v124 offset:9216
	ds_read_b64 v[46:47], v125 offset:11776
	s_waitcnt vmcnt(6) lgkmcnt(0)
	s_barrier
	s_add_u32 s24, s10, 0xf000
	s_addc_u32 s25, s11, 0
	s_mov_b32 m0, s13
	s_nop 0
	global_load_lds_dwordx4 v124, s[24:25]
	s_add_u32 s26, s24, 0x2000
	s_addc_u32 s27, s25, 0
	s_mov_b32 m0, s20
	s_nop 0
	global_load_lds_dwordx4 v124, s[26:27]
	v_mfma_f32_32x32x64_f8f6f4 v[64:79], v[24:29], v[96:101], 0 cbsz:2 blgp:2
	ds_read_b128 v[0:3], v124 offset:12288
	ds_read_b64 v[4:5], v125 offset:16384
	ds_read_b128 v[6:9], v124 offset:13312
	ds_read_b64 v[10:11], v125 offset:16896
	ds_read_b128 v[24:27], v124 offset:18432
	ds_read_b64 v[28:29], v125 offset:22528
	v_mfma_f32_32x32x64_f8f6f4 v[64:79], v[30:35], v[102:107], v[64:79] cbsz:2 blgp:2
	ds_read_b128 v[12:15], v124 offset:14336
	ds_read_b64 v[16:17], v125 offset:17408
	ds_read_b128 v[18:21], v124 offset:15360
	ds_read_b64 v[22:23], v125 offset:17920
	ds_read_b128 v[30:33], v124 offset:19456
	ds_read_b64 v[34:35], v125 offset:23040
	v_exp_f32_e32 v48, v48
	v_exp_f32_e32 v49, v49
	v_exp_f32_e32 v50, v50
	v_exp_f32_e32 v51, v51
	v_mfma_f32_32x32x64_f8f6f4 v[64:79], v[36:41], v[108:113], v[64:79] cbsz:2 blgp:2
	ds_read_b128 v[36:39], v124 offset:20480
	ds_read_b64 v[40:41], v125 offset:23552
	v_exp_f32_e32 v52, v52
	v_exp_f32_e32 v53, v53
	v_exp_f32_e32 v54, v54
	v_exp_f32_e32 v55, v55
	v_pk_add_f32 v[120:121], v[120:121], v[48:49]
	v_pk_add_f32 v[122:123], v[122:123], v[50:51]
	v_mfma_f32_32x32x64_f8f6f4 v[64:79], v[42:47], v[114:119], v[64:79] cbsz:2 blgp:2
	ds_read_b128 v[42:45], v124 offset:21504
	ds_read_b64 v[46:47], v125 offset:24064
	v_exp_f32_e32 v56, v56
	v_exp_f32_e32 v57, v57
	v_exp_f32_e32 v58, v58
	v_exp_f32_e32 v59, v59
	v_pk_add_f32 v[120:121], v[120:121], v[52:53]
	v_pk_add_f32 v[122:123], v[122:123], v[54:55]
	s_waitcnt vmcnt(6) lgkmcnt(6)
	s_barrier
	v_mfma_f32_32x32x64_f8f6f4 v[80:95], v[0:5], v[96:101], 0 cbsz:2 blgp:2
	ds_read_b128 v[0:3], v124 offset:24576
	ds_read_b64 v[4:5], v125 offset:28672
	v_exp_f32_e32 v60, v60
	v_exp_f32_e32 v61, v61
	v_exp_f32_e32 v62, v62
	v_exp_f32_e32 v63, v63
	v_pk_add_f32 v[120:121], v[120:121], v[56:57]
	v_pk_add_f32 v[122:123], v[122:123], v[58:59]
	v_mfma_f32_32x32x64_f8f6f4 v[80:95], v[6:11], v[102:107], v[80:95] cbsz:2 blgp:2
	ds_read_b128 v[6:9], v124 offset:25600
	ds_read_b64 v[10:11], v125 offset:29184
	v_exp_f32_e32 v64, v64
	v_exp_f32_e32 v65, v65
	v_exp_f32_e32 v66, v66
	v_exp_f32_e32 v67, v67
	v_pk_add_f32 v[120:121], v[120:121], v[60:61]
	v_pk_add_f32 v[122:123], v[122:123], v[62:63]
	v_mfma_f32_32x32x64_f8f6f4 v[80:95], v[12:17], v[108:113], v[80:95] cbsz:2 blgp:2
	ds_read_b128 v[12:15], v124 offset:26624
	ds_read_b64 v[16:17], v125 offset:29696
	v_exp_f32_e32 v68, v68
	v_exp_f32_e32 v69, v69
	v_exp_f32_e32 v70, v70
	v_exp_f32_e32 v71, v71
	v_pk_add_f32 v[120:121], v[120:121], v[64:65]
	v_pk_add_f32 v[122:123], v[122:123], v[66:67]
	v_mfma_f32_32x32x64_f8f6f4 v[80:95], v[18:23], v[114:119], v[80:95] cbsz:2 blgp:2
	ds_read_b128 v[18:21], v124 offset:27648
	ds_read_b64 v[22:23], v125 offset:30208
	v_exp_f32_e32 v72, v72
	v_exp_f32_e32 v73, v73
	v_exp_f32_e32 v74, v74
	v_exp_f32_e32 v75, v75
	v_pk_add_f32 v[120:121], v[120:121], v[68:69]
	v_pk_add_f32 v[122:123], v[122:123], v[70:71]
	s_waitcnt lgkmcnt(8)
	v_mfma_f32_32x32x64_f8f6f4 v[48:63], v[24:29], v[96:101], 0 cbsz:2 blgp:2
	ds_read_b128 v[24:27], v124 offset:30720
	ds_read_b64 v[28:29], v125 offset:34816
	v_exp_f32_e32 v76, v76
	v_exp_f32_e32 v77, v77
	v_exp_f32_e32 v78, v78
	v_exp_f32_e32 v79, v79
	v_pk_add_f32 v[120:121], v[120:121], v[72:73]
	v_pk_add_f32 v[122:123], v[122:123], v[74:75]
	v_mfma_f32_32x32x64_f8f6f4 v[48:63], v[30:35], v[102:107], v[48:63] cbsz:2 blgp:2
	ds_read_b128 v[30:33], v124 offset:31744
	ds_read_b64 v[34:35], v125 offset:35328
	v_exp_f32_e32 v80, v80
	v_exp_f32_e32 v81, v81
	v_exp_f32_e32 v82, v82
	v_exp_f32_e32 v83, v83
	v_pk_add_f32 v[120:121], v[120:121], v[76:77]
	v_pk_add_f32 v[122:123], v[122:123], v[78:79]
	v_mfma_f32_32x32x64_f8f6f4 v[48:63], v[36:41], v[108:113], v[48:63] cbsz:2 blgp:2
	ds_read_b128 v[36:39], v124 offset:32768
	ds_read_b64 v[40:41], v125 offset:35840
	v_exp_f32_e32 v84, v84
	v_exp_f32_e32 v85, v85
	v_exp_f32_e32 v86, v86
	v_exp_f32_e32 v87, v87
	v_pk_add_f32 v[120:121], v[120:121], v[80:81]
	v_pk_add_f32 v[122:123], v[122:123], v[82:83]
	v_mfma_f32_32x32x64_f8f6f4 v[48:63], v[42:47], v[114:119], v[48:63] cbsz:2 blgp:2
	ds_read_b128 v[42:45], v124 offset:33792
	ds_read_b64 v[46:47], v125 offset:36352
	v_exp_f32_e32 v88, v88
	v_exp_f32_e32 v89, v89
	v_exp_f32_e32 v90, v90
	v_exp_f32_e32 v91, v91
	v_pk_add_f32 v[120:121], v[120:121], v[84:85]
	v_pk_add_f32 v[122:123], v[122:123], v[86:87]
	s_setprio 2
	s_waitcnt vmcnt(4) lgkmcnt(8)
	s_barrier
	v_mfma_f32_32x32x64_f8f6f4 v[64:79], v[0:5], v[96:101], 0 cbsz:2 blgp:2
	ds_read_b128 v[0:3], v124 offset:36864
	ds_read_b64 v[4:5], v125 offset:40960
	v_exp_f32_e32 v92, v92
	v_exp_f32_e32 v93, v93
	v_exp_f32_e32 v94, v94
	v_exp_f32_e32 v95, v95
	v_pk_add_f32 v[120:121], v[120:121], v[88:89]
	v_pk_add_f32 v[122:123], v[122:123], v[90:91]
	v_mfma_f32_32x32x64_f8f6f4 v[64:79], v[6:11], v[102:107], v[64:79] cbsz:2 blgp:2
	ds_read_b128 v[6:9], v124 offset:37888
	ds_read_b64 v[10:11], v125 offset:41472
	v_exp_f32_e32 v48, v48
	v_exp_f32_e32 v49, v49
	v_exp_f32_e32 v50, v50
	v_exp_f32_e32 v51, v51
	v_pk_add_f32 v[120:121], v[120:121], v[92:93]
	v_pk_add_f32 v[122:123], v[122:123], v[94:95]
	v_mfma_f32_32x32x64_f8f6f4 v[64:79], v[12:17], v[108:113], v[64:79] cbsz:2 blgp:2
	ds_read_b128 v[12:15], v124 offset:38912
	ds_read_b64 v[16:17], v125 offset:41984
	v_exp_f32_e32 v52, v52
	v_exp_f32_e32 v53, v53
	v_exp_f32_e32 v54, v54
	v_exp_f32_e32 v55, v55
	v_pk_add_f32 v[120:121], v[120:121], v[48:49]
	v_pk_add_f32 v[122:123], v[122:123], v[50:51]
	v_mfma_f32_32x32x64_f8f6f4 v[64:79], v[18:23], v[114:119], v[64:79] cbsz:2 blgp:2
	ds_read_b128 v[18:21], v124 offset:39936
	ds_read_b64 v[22:23], v125 offset:42496
	v_exp_f32_e32 v56, v56
	v_exp_f32_e32 v57, v57
	v_exp_f32_e32 v58, v58
	v_exp_f32_e32 v59, v59
	v_pk_add_f32 v[120:121], v[120:121], v[52:53]
	v_pk_add_f32 v[122:123], v[122:123], v[54:55]
	s_waitcnt lgkmcnt(8)
	v_mfma_f32_32x32x64_f8f6f4 v[80:95], v[24:29], v[96:101], 0 cbsz:2 blgp:2
	ds_read_b128 v[24:27], v124 offset:43008
	ds_read_b64 v[28:29], v125 offset:47104
	v_exp_f32_e32 v60, v60
	v_exp_f32_e32 v61, v61
	v_exp_f32_e32 v62, v62
	v_exp_f32_e32 v63, v63
	v_pk_add_f32 v[120:121], v[120:121], v[56:57]
	v_pk_add_f32 v[122:123], v[122:123], v[58:59]
	v_mfma_f32_32x32x64_f8f6f4 v[80:95], v[30:35], v[102:107], v[80:95] cbsz:2 blgp:2
	ds_read_b128 v[30:33], v124 offset:44032
	ds_read_b64 v[34:35], v125 offset:47616
	v_exp_f32_e32 v64, v64
	v_exp_f32_e32 v65, v65
	v_exp_f32_e32 v66, v66
	v_exp_f32_e32 v67, v67
	v_pk_add_f32 v[120:121], v[120:121], v[60:61]
	v_pk_add_f32 v[122:123], v[122:123], v[62:63]
	v_mfma_f32_32x32x64_f8f6f4 v[80:95], v[36:41], v[108:113], v[80:95] cbsz:2 blgp:2
	ds_read_b128 v[36:39], v124 offset:45056
	ds_read_b64 v[40:41], v125 offset:48128
	v_exp_f32_e32 v68, v68
	v_exp_f32_e32 v69, v69
	v_exp_f32_e32 v70, v70
	v_exp_f32_e32 v71, v71
	v_pk_add_f32 v[120:121], v[120:121], v[64:65]
	v_pk_add_f32 v[122:123], v[122:123], v[66:67]
	v_mfma_f32_32x32x64_f8f6f4 v[80:95], v[42:47], v[114:119], v[80:95] cbsz:2 blgp:2
	ds_read_b128 v[42:45], v124 offset:46080
	ds_read_b64 v[46:47], v125 offset:48640
	v_exp_f32_e32 v72, v72
	v_exp_f32_e32 v73, v73
	v_exp_f32_e32 v74, v74
	v_exp_f32_e32 v75, v75
	v_pk_add_f32 v[120:121], v[120:121], v[68:69]
	v_pk_add_f32 v[122:123], v[122:123], v[70:71]
	s_waitcnt vmcnt(2) lgkmcnt(8)
	s_barrier
	v_mfma_f32_32x32x64_f8f6f4 v[48:63], v[0:5], v[96:101], 0 cbsz:2 blgp:2
	ds_read_b128 v[0:3], v124 offset:49152
	ds_read_b64 v[4:5], v125 offset:53248
	v_exp_f32_e32 v76, v76
	v_exp_f32_e32 v77, v77
	v_exp_f32_e32 v78, v78
	v_exp_f32_e32 v79, v79
	v_pk_add_f32 v[120:121], v[120:121], v[72:73]
	v_pk_add_f32 v[122:123], v[122:123], v[74:75]
	v_mfma_f32_32x32x64_f8f6f4 v[48:63], v[6:11], v[102:107], v[48:63] cbsz:2 blgp:2
	ds_read_b128 v[6:9], v124 offset:50176
	ds_read_b64 v[10:11], v125 offset:53760
	v_exp_f32_e32 v80, v80
	v_exp_f32_e32 v81, v81
	v_exp_f32_e32 v82, v82
	v_exp_f32_e32 v83, v83
	v_pk_add_f32 v[120:121], v[120:121], v[76:77]
	v_pk_add_f32 v[122:123], v[122:123], v[78:79]
	v_mfma_f32_32x32x64_f8f6f4 v[48:63], v[12:17], v[108:113], v[48:63] cbsz:2 blgp:2
	ds_read_b128 v[12:15], v124 offset:51200
	ds_read_b64 v[16:17], v125 offset:54272
	v_exp_f32_e32 v84, v84
	v_exp_f32_e32 v85, v85
	v_exp_f32_e32 v86, v86
	v_exp_f32_e32 v87, v87
	v_pk_add_f32 v[120:121], v[120:121], v[80:81]
	v_pk_add_f32 v[122:123], v[122:123], v[82:83]
	v_mfma_f32_32x32x64_f8f6f4 v[48:63], v[18:23], v[114:119], v[48:63] cbsz:2 blgp:2
	ds_read_b128 v[18:21], v124 offset:52224
	ds_read_b64 v[22:23], v125 offset:54784
	v_exp_f32_e32 v88, v88
	v_exp_f32_e32 v89, v89
	v_exp_f32_e32 v90, v90
	v_exp_f32_e32 v91, v91
	v_pk_add_f32 v[120:121], v[120:121], v[84:85]
	v_pk_add_f32 v[122:123], v[122:123], v[86:87]
	s_waitcnt lgkmcnt(8)
	v_mfma_f32_32x32x64_f8f6f4 v[64:79], v[24:29], v[96:101], 0 cbsz:2 blgp:2
	ds_read_b128 v[24:27], v124 offset:55296
	ds_read_b64 v[28:29], v125 offset:59392
	v_exp_f32_e32 v92, v92
	v_exp_f32_e32 v93, v93
	v_exp_f32_e32 v94, v94
	v_exp_f32_e32 v95, v95
	v_pk_add_f32 v[120:121], v[120:121], v[88:89]
	v_pk_add_f32 v[122:123], v[122:123], v[90:91]
	v_mfma_f32_32x32x64_f8f6f4 v[64:79], v[30:35], v[102:107], v[64:79] cbsz:2 blgp:2
	ds_read_b128 v[30:33], v124 offset:56320
	ds_read_b64 v[34:35], v125 offset:59904
	v_exp_f32_e32 v48, v48
	v_exp_f32_e32 v49, v49
	v_exp_f32_e32 v50, v50
	v_exp_f32_e32 v51, v51
	v_pk_add_f32 v[120:121], v[120:121], v[92:93]
	v_pk_add_f32 v[122:123], v[122:123], v[94:95]
	v_mfma_f32_32x32x64_f8f6f4 v[64:79], v[36:41], v[108:113], v[64:79] cbsz:2 blgp:2
	ds_read_b128 v[36:39], v124 offset:57344
	ds_read_b64 v[40:41], v125 offset:60416
	v_exp_f32_e32 v52, v52
	v_exp_f32_e32 v53, v53
	v_exp_f32_e32 v54, v54
	v_exp_f32_e32 v55, v55
	v_pk_add_f32 v[120:121], v[120:121], v[48:49]
	v_pk_add_f32 v[122:123], v[122:123], v[50:51]
	v_mfma_f32_32x32x64_f8f6f4 v[64:79], v[42:47], v[114:119], v[64:79] cbsz:2 blgp:2
	ds_read_b128 v[42:45], v124 offset:58368
	ds_read_b64 v[46:47], v125 offset:60928
	v_exp_f32_e32 v56, v56
	v_exp_f32_e32 v57, v57
	v_exp_f32_e32 v58, v58
	v_exp_f32_e32 v59, v59
	v_pk_add_f32 v[120:121], v[120:121], v[52:53]
	v_pk_add_f32 v[122:123], v[122:123], v[54:55]
	s_setprio 1
	s_waitcnt vmcnt(0) lgkmcnt(8)
	s_barrier
	v_mfma_f32_32x32x64_f8f6f4 v[80:95], v[0:5], v[96:101], 0 cbsz:2 blgp:2
	ds_read_b128 v[0:3], v124
	ds_read_b64 v[4:5], v125 offset:4096
	v_exp_f32_e32 v60, v60
	v_exp_f32_e32 v61, v61
	v_exp_f32_e32 v62, v62
	v_exp_f32_e32 v63, v63
	v_pk_add_f32 v[120:121], v[120:121], v[56:57]
	v_pk_add_f32 v[122:123], v[122:123], v[58:59]
	v_mfma_f32_32x32x64_f8f6f4 v[80:95], v[6:11], v[102:107], v[80:95] cbsz:2 blgp:2
	ds_read_b128 v[6:9], v124 offset:1024
	ds_read_b64 v[10:11], v125 offset:4608
	v_exp_f32_e32 v64, v64
	v_exp_f32_e32 v65, v65
	v_exp_f32_e32 v66, v66
	v_exp_f32_e32 v67, v67
	v_pk_add_f32 v[120:121], v[120:121], v[60:61]
	v_pk_add_f32 v[122:123], v[122:123], v[62:63]
	v_mfma_f32_32x32x64_f8f6f4 v[80:95], v[12:17], v[108:113], v[80:95] cbsz:2 blgp:2
	ds_read_b128 v[12:15], v124 offset:2048
	ds_read_b64 v[16:17], v125 offset:5120
	v_exp_f32_e32 v68, v68
	v_exp_f32_e32 v69, v69
	v_exp_f32_e32 v70, v70
	v_exp_f32_e32 v71, v71
	v_pk_add_f32 v[120:121], v[120:121], v[64:65]
	v_pk_add_f32 v[122:123], v[122:123], v[66:67]
	v_mfma_f32_32x32x64_f8f6f4 v[80:95], v[18:23], v[114:119], v[80:95] cbsz:2 blgp:2
	ds_read_b128 v[18:21], v124 offset:3072
	ds_read_b64 v[22:23], v125 offset:5632
	v_exp_f32_e32 v72, v72
	v_exp_f32_e32 v73, v73
	v_exp_f32_e32 v74, v74
	v_exp_f32_e32 v75, v75
	v_pk_add_f32 v[120:121], v[120:121], v[68:69]
	v_pk_add_f32 v[122:123], v[122:123], v[70:71]
	s_waitcnt lgkmcnt(8)
	v_mfma_f32_32x32x64_f8f6f4 v[48:63], v[24:29], v[96:101], 0 cbsz:2 blgp:2
	ds_read_b128 v[24:27], v124 offset:6144
	ds_read_b64 v[28:29], v125 offset:10240
	v_exp_f32_e32 v76, v76
	v_exp_f32_e32 v77, v77
	v_exp_f32_e32 v78, v78
	v_exp_f32_e32 v79, v79
	v_pk_add_f32 v[120:121], v[120:121], v[72:73]
	v_pk_add_f32 v[122:123], v[122:123], v[74:75]
	v_mfma_f32_32x32x64_f8f6f4 v[48:63], v[30:35], v[102:107], v[48:63] cbsz:2 blgp:2
	ds_read_b128 v[30:33], v124 offset:7168
	ds_read_b64 v[34:35], v125 offset:10752
	v_exp_f32_e32 v80, v80
	v_exp_f32_e32 v81, v81
	v_exp_f32_e32 v82, v82
	v_exp_f32_e32 v83, v83
	v_pk_add_f32 v[120:121], v[120:121], v[76:77]
	v_pk_add_f32 v[122:123], v[122:123], v[78:79]
	s_cmp_lg_u32 s8, 10
	s_cbranch_scc1 .Lmk_nosplit_a
	v_add_f32_e32 v127, v120, v121
	v_add_f32_e32 v126, v122, v123
	v_mov_b32_e32 v120, 0
	v_mov_b32_e32 v121, 0
	v_mov_b32_e32 v122, 0
	v_mov_b32_e32 v123, 0
	v_add_f32_e32 v127, v127, v126
.Lmk_nosplit_a:
	v_mfma_f32_32x32x64_f8f6f4 v[48:63], v[36:41], v[108:113], v[48:63] cbsz:2 blgp:2
	ds_read_b128 v[36:39], v124 offset:8192
	ds_read_b64 v[40:41], v125 offset:11264
	v_exp_f32_e32 v84, v84
	v_exp_f32_e32 v85, v85
	v_exp_f32_e32 v86, v86
	v_exp_f32_e32 v87, v87
	v_pk_add_f32 v[120:121], v[120:121], v[80:81]
	v_pk_add_f32 v[122:123], v[122:123], v[82:83]
	v_mfma_f32_32x32x64_f8f6f4 v[48:63], v[42:47], v[114:119], v[48:63] cbsz:2 blgp:2
	ds_read_b128 v[42:45], v124 offset:9216
	ds_read_b64 v[46:47], v125 offset:11776
	v_exp_f32_e32 v88, v88
	v_exp_f32_e32 v89, v89
	v_exp_f32_e32 v90, v90
	v_exp_f32_e32 v91, v91
	v_pk_add_f32 v[120:121], v[120:121], v[84:85]
	v_pk_add_f32 v[122:123], v[122:123], v[86:87]
	s_setprio 0
	s_waitcnt lgkmcnt(8)
	v_mfma_f32_32x32x64_f8f6f4 v[64:79], v[0:5], v[96:101], 0 cbsz:2 blgp:2
	v_exp_f32_e32 v92, v92
	v_exp_f32_e32 v93, v93
	v_exp_f32_e32 v94, v94
	v_exp_f32_e32 v95, v95
	v_pk_add_f32 v[120:121], v[120:121], v[88:89]
	v_pk_add_f32 v[122:123], v[122:123], v[90:91]
	v_mfma_f32_32x32x64_f8f6f4 v[64:79], v[6:11], v[102:107], v[64:79] cbsz:2 blgp:2
	v_exp_f32_e32 v48, v48
	v_exp_f32_e32 v49, v49
	v_exp_f32_e32 v50, v50
	v_exp_f32_e32 v51, v51
	v_pk_add_f32 v[120:121], v[120:121], v[92:93]
	v_pk_add_f32 v[122:123], v[122:123], v[94:95]
	v_mfma_f32_32x32x64_f8f6f4 v[64:79], v[12:17], v[108:113], v[64:79] cbsz:2 blgp:2
	v_exp_f32_e32 v52, v52
	v_exp_f32_e32 v53, v53
	v_exp_f32_e32 v54, v54
	v_exp_f32_e32 v55, v55
	v_pk_add_f32 v[120:121], v[120:121], v[48:49]
	v_pk_add_f32 v[122:123], v[122:123], v[50:51]
	v_mfma_f32_32x32x64_f8f6f4 v[64:79], v[18:23], v[114:119], v[64:79] cbsz:2 blgp:2
	v_exp_f32_e32 v56, v56
	v_exp_f32_e32 v57, v57
	v_exp_f32_e32 v58, v58
	v_exp_f32_e32 v59, v59
	v_pk_add_f32 v[120:121], v[120:121], v[52:53]
	v_pk_add_f32 v[122:123], v[122:123], v[54:55]
	s_waitcnt lgkmcnt(0)
	v_mfma_f32_32x32x64_f8f6f4 v[80:95], v[24:29], v[96:101], 0 cbsz:2 blgp:2
	v_exp_f32_e32 v60, v60
	v_exp_f32_e32 v61, v61
	v_exp_f32_e32 v62, v62
	v_exp_f32_e32 v63, v63
	v_pk_add_f32 v[120:121], v[120:121], v[56:57]
	v_pk_add_f32 v[122:123], v[122:123], v[58:59]
	v_mfma_f32_32x32x64_f8f6f4 v[80:95], v[30:35], v[102:107], v[80:95] cbsz:2 blgp:2
	v_exp_f32_e32 v64, v64
	v_exp_f32_e32 v65, v65
	v_exp_f32_e32 v66, v66
	v_exp_f32_e32 v67, v67
	v_pk_add_f32 v[120:121], v[120:121], v[60:61]
	v_pk_add_f32 v[122:123], v[122:123], v[62:63]
	v_mfma_f32_32x32x64_f8f6f4 v[80:95], v[36:41], v[108:113], v[80:95] cbsz:2 blgp:2
	v_exp_f32_e32 v68, v68
	v_exp_f32_e32 v69, v69
	v_exp_f32_e32 v70, v70
	v_exp_f32_e32 v71, v71
	v_pk_add_f32 v[120:121], v[120:121], v[64:65]
	v_pk_add_f32 v[122:123], v[122:123], v[66:67]
	v_mfma_f32_32x32x64_f8f6f4 v[80:95], v[42:47], v[114:119], v[80:95] cbsz:2 blgp:2
	v_exp_f32_e32 v72, v72
	v_exp_f32_e32 v73, v73
	v_exp_f32_e32 v74, v74
	v_exp_f32_e32 v75, v75
	v_pk_add_f32 v[120:121], v[120:121], v[68:69]
	v_pk_add_f32 v[122:123], v[122:123], v[70:71]
	v_exp_f32_e32 v76, v76
	v_exp_f32_e32 v77, v77
	v_exp_f32_e32 v78, v78
	v_exp_f32_e32 v79, v79
	v_pk_add_f32 v[120:121], v[120:121], v[72:73]
	v_pk_add_f32 v[122:123], v[122:123], v[74:75]
	s_nop 1
	v_exp_f32_e32 v80, v80
	v_exp_f32_e32 v81, v81
	v_exp_f32_e32 v82, v82
	v_exp_f32_e32 v83, v83
	v_pk_add_f32 v[120:121], v[120:121], v[76:77]
	v_pk_add_f32 v[122:123], v[122:123], v[78:79]
	v_exp_f32_e32 v84, v84
	v_exp_f32_e32 v85, v85
	v_exp_f32_e32 v86, v86
	v_exp_f32_e32 v87, v87
	v_pk_add_f32 v[120:121], v[120:121], v[80:81]
	v_pk_add_f32 v[122:123], v[122:123], v[82:83]
	v_exp_f32_e32 v88, v88
	v_exp_f32_e32 v89, v89
	v_exp_f32_e32 v90, v90
	v_exp_f32_e32 v91, v91
	v_pk_add_f32 v[120:121], v[120:121], v[84:85]
	v_pk_add_f32 v[122:123], v[122:123], v[86:87]
	v_exp_f32_e32 v92, v92
	v_exp_f32_e32 v93, v93
	v_exp_f32_e32 v94, v94
	v_exp_f32_e32 v95, v95
	v_pk_add_f32 v[120:121], v[120:121], v[88:89]
	v_pk_add_f32 v[122:123], v[122:123], v[90:91]
	v_pk_add_f32 v[120:121], v[120:121], v[92:93]
	v_pk_add_f32 v[122:123], v[122:123], v[94:95]
	v_add_f32_e32 v120, v120, v121
	v_add_f32_e32 v122, v122, v123
	v_lshrrev_b32_e32 v126, 2, v124
	v_add_f32_e32 v120, v120, v122
	v_xor_b32_e32 v125, 0x80, v126
	s_mov_b64 s[4:5], s[30:31]
	s_mov_b64 s[6:7], s[32:33]
	ds_bpermute_b32 v122, v125, v120
	ds_bpermute_b32 v123, v125, v127
	s_lshl_b32 s14, s14, 7
	v_add_u32_e32 v126, s14, v126
	v_cmp_gt_u32_e32 vcc, 0x200, v124
	s_and_saveexec_b64 s[16:17], vcc
	s_cbranch_execz .Lmk_end_a
	s_waitcnt lgkmcnt(0)
	v_add_f32_e32 v120, v120, v122
	v_add_f32_e32 v127, v127, v123
	s_cmp_lt_u32 s8, 10
	s_cbranch_scc1 .Lmk_pos_only_a
	s_cmp_eq_u32 s8, 10
	s_cbranch_scc0 .Lmk_neg_only_a
	global_atomic_add_f32 v126, v127, s[4:5]

.Lmk_vb:
	s_mov_b32 m0, s13
	s_nop 0
	global_load_lds_dwordx4 v124, s[10:11]
	global_load_dwordx4 v[96:99], v124, s[18:19]
	global_load_dwordx2 v[100:101], v125, s[22:23]
	global_load_dwordx4 v[102:105], v124, s[18:19] offset:1024
	global_load_dwordx2 v[106:107], v125, s[22:23] offset:512
	global_load_dwordx4 v[108:111], v124, s[18:19] offset:2048
	global_load_dwordx2 v[112:113], v125, s[22:23] offset:1024
	global_load_dwordx4 v[114:117], v124, s[18:19] offset:3072
	global_load_dwordx2 v[118:119], v125, s[22:23] offset:1536
	s_add_u32 s24, s10, 0x3000
	s_addc_u32 s25, s11, 0
	s_add_u32 s26, s13, 0x3000
	s_mov_b32 m0, s26
	s_nop 0
	global_load_lds_dwordx4 v124, s[24:25]
	s_add_u32 s24, s10, 0x6000
	s_addc_u32 s25, s11, 0
	s_add_u32 s26, s13, 0x6000
	s_mov_b32 m0, s26
	s_nop 0
	global_load_lds_dwordx4 v124, s[24:25]
	s_add_u32 s24, s10, 0x9000
	s_addc_u32 s25, s11, 0
	s_add_u32 s26, s13, 0x9000
	s_mov_b32 m0, s26
	s_nop 0
	global_load_lds_dwordx4 v124, s[24:25]
	s_add_u32 s24, s10, 0xc000
	s_addc_u32 s25, s11, 0
	s_add_u32 s26, s13, 0xc000
	s_mov_b32 m0, s26
	s_nop 0
	global_load_lds_dwordx4 v124, s[24:25]
	s_waitcnt vmcnt(4)
	s_barrier
	ds_read_b128 v[0:3], v124
	ds_read_b64 v[4:5], v125 offset:4096
	ds_read_b128 v[6:9], v124 offset:1024
	ds_read_b64 v[10:11], v125 offset:4608
	ds_read_b128 v[12:15], v124 offset:2048
	ds_read_b64 v[16:17], v125 offset:5120
	ds_read_b128 v[18:21], v124 offset:3072
	ds_read_b64 v[22:23], v125 offset:5632
	s_waitcnt lgkmcnt(0)
	s_setprio 3
	v_mfma_f32_32x32x64_f8f6f4 v[48:63], v[0:5], v[96:101], 0 cbsz:2 blgp:2
	ds_read_b128 v[24:27], v124 offset:6144
	ds_read_b64 v[28:29], v125 offset:10240
	v_mfma_f32_32x32x64_f8f6f4 v[48:63], v[6:11], v[102:107], v[48:63] cbsz:2 blgp:2
	ds_read_b128 v[30:33], v124 offset:7168
	ds_read_b64 v[34:35], v125 offset:10752
	v_mfma_f32_32x32x64_f8f6f4 v[48:63], v[12:17], v[108:113], v[48:63] cbsz:2 blgp:2
	ds_read_b128 v[36:39], v124 offset:8192
	ds_read_b64 v[40:41], v125 offset:11264
	v_mfma_f32_32x32x64_f8f6f4 v[48:63], v[18:23], v[114:119], v[48:63] cbsz:2 blgp:2
	ds_read_b128 v[42:45], v124 offset:9216
	ds_read_b64 v[46:47], v125 offset:11776
	s_waitcnt vmcnt(3) lgkmcnt(0)
	s_barrier
	s_add_u32 s24, s10, 0xf000
	s_addc_u32 s25, s11, 0
	s_mov_b32 m0, s13
	s_nop 0
	global_load_lds_dwordx4 v124, s[24:25]
	v_mfma_f32_32x32x64_f8f6f4 v[64:79], v[24:29], v[96:101], 0 cbsz:2 blgp:2
	ds_read_b128 v[0:3], v124 offset:12288
	ds_read_b64 v[4:5], v125 offset:16384
	ds_read_b128 v[6:9], v124 offset:13312
	ds_read_b64 v[10:11], v125 offset:16896
	ds_read_b128 v[24:27], v124 offset:18432
	ds_read_b64 v[28:29], v125 offset:22528
	v_mfma_f32_32x32x64_f8f6f4 v[64:79], v[30:35], v[102:107], v[64:79] cbsz:2 blgp:2
	ds_read_b128 v[12:15], v124 offset:14336
	ds_read_b64 v[16:17], v125 offset:17408
	ds_read_b128 v[18:21], v124 offset:15360
	ds_read_b64 v[22:23], v125 offset:17920
	ds_read_b128 v[30:33], v124 offset:19456
	ds_read_b64 v[34:35], v125 offset:23040
	v_exp_f32_e32 v48, v48
	v_exp_f32_e32 v49, v49
	v_exp_f32_e32 v50, v50
	v_exp_f32_e32 v51, v51
	v_mfma_f32_32x32x64_f8f6f4 v[64:79], v[36:41], v[108:113], v[64:79] cbsz:2 blgp:2
	ds_read_b128 v[36:39], v124 offset:20480
	ds_read_b64 v[40:41], v125 offset:23552
	v_exp_f32_e32 v52, v52
	v_exp_f32_e32 v53, v53
	v_exp_f32_e32 v54, v54
	v_exp_f32_e32 v55, v55
	v_pk_add_f32 v[120:121], v[120:121], v[48:49]
	v_pk_add_f32 v[122:123], v[122:123], v[50:51]
	v_mfma_f32_32x32x64_f8f6f4 v[64:79], v[42:47], v[114:119], v[64:79] cbsz:2 blgp:2
	ds_read_b128 v[42:45], v124 offset:21504
	ds_read_b64 v[46:47], v125 offset:24064
	v_exp_f32_e32 v56, v56
	v_exp_f32_e32 v57, v57
	v_exp_f32_e32 v58, v58
	v_exp_f32_e32 v59, v59
	v_pk_add_f32 v[120:121], v[120:121], v[52:53]
	v_pk_add_f32 v[122:123], v[122:123], v[54:55]
	s_waitcnt vmcnt(3) lgkmcnt(6)
	s_barrier
	v_mfma_f32_32x32x64_f8f6f4 v[80:95], v[0:5], v[96:101], 0 cbsz:2 blgp:2
	ds_read_b128 v[0:3], v124 offset:24576
	ds_read_b64 v[4:5], v125 offset:28672
	v_exp_f32_e32 v60, v60
	v_exp_f32_e32 v61, v61
	v_exp_f32_e32 v62, v62
	v_exp_f32_e32 v63, v63
	v_pk_add_f32 v[120:121], v[120:121], v[56:57]
	v_pk_add_f32 v[122:123], v[122:123], v[58:59]
	v_mfma_f32_32x32x64_f8f6f4 v[80:95], v[6:11], v[102:107], v[80:95] cbsz:2 blgp:2
	ds_read_b128 v[6:9], v124 offset:25600
	ds_read_b64 v[10:11], v125 offset:29184
	v_exp_f32_e32 v64, v64
	v_exp_f32_e32 v65, v65
	v_exp_f32_e32 v66, v66
	v_exp_f32_e32 v67, v67
	v_pk_add_f32 v[120:121], v[120:121], v[60:61]
	v_pk_add_f32 v[122:123], v[122:123], v[62:63]
	v_mfma_f32_32x32x64_f8f6f4 v[80:95], v[12:17], v[108:113], v[80:95] cbsz:2 blgp:2
	ds_read_b128 v[12:15], v124 offset:26624
	ds_read_b64 v[16:17], v125 offset:29696
	v_exp_f32_e32 v68, v68
	v_exp_f32_e32 v69, v69
	v_exp_f32_e32 v70, v70
	v_exp_f32_e32 v71, v71
	v_pk_add_f32 v[120:121], v[120:121], v[64:65]
	v_pk_add_f32 v[122:123], v[122:123], v[66:67]
	v_mfma_f32_32x32x64_f8f6f4 v[80:95], v[18:23], v[114:119], v[80:95] cbsz:2 blgp:2
	ds_read_b128 v[18:21], v124 offset:27648
	ds_read_b64 v[22:23], v125 offset:30208
	v_exp_f32_e32 v72, v72
	v_exp_f32_e32 v73, v73
	v_exp_f32_e32 v74, v74
	v_exp_f32_e32 v75, v75
	v_pk_add_f32 v[120:121], v[120:121], v[68:69]
	v_pk_add_f32 v[122:123], v[122:123], v[70:71]
	s_waitcnt lgkmcnt(8)
	v_mfma_f32_32x32x64_f8f6f4 v[48:63], v[24:29], v[96:101], 0 cbsz:2 blgp:2
	ds_read_b128 v[24:27], v124 offset:30720
	ds_read_b64 v[28:29], v125 offset:34816
	v_exp_f32_e32 v76, v76
	v_exp_f32_e32 v77, v77
	v_exp_f32_e32 v78, v78
	v_exp_f32_e32 v79, v79
	v_pk_add_f32 v[120:121], v[120:121], v[72:73]
	v_pk_add_f32 v[122:123], v[122:123], v[74:75]
	v_mfma_f32_32x32x64_f8f6f4 v[48:63], v[30:35], v[102:107], v[48:63] cbsz:2 blgp:2
	ds_read_b128 v[30:33], v124 offset:31744
	ds_read_b64 v[34:35], v125 offset:35328
	v_exp_f32_e32 v80, v80
	v_exp_f32_e32 v81, v81
	v_exp_f32_e32 v82, v82
	v_exp_f32_e32 v83, v83
	v_pk_add_f32 v[120:121], v[120:121], v[76:77]
	v_pk_add_f32 v[122:123], v[122:123], v[78:79]
	v_mfma_f32_32x32x64_f8f6f4 v[48:63], v[36:41], v[108:113], v[48:63] cbsz:2 blgp:2
	ds_read_b128 v[36:39], v124 offset:32768
	ds_read_b64 v[40:41], v125 offset:35840
	v_exp_f32_e32 v84, v84
	v_exp_f32_e32 v85, v85
	v_exp_f32_e32 v86, v86
	v_exp_f32_e32 v87, v87
	v_pk_add_f32 v[120:121], v[120:121], v[80:81]
	v_pk_add_f32 v[122:123], v[122:123], v[82:83]
	v_mfma_f32_32x32x64_f8f6f4 v[48:63], v[42:47], v[114:119], v[48:63] cbsz:2 blgp:2
	ds_read_b128 v[42:45], v124 offset:33792
	ds_read_b64 v[46:47], v125 offset:36352
	v_exp_f32_e32 v88, v88
	v_exp_f32_e32 v89, v89
	v_exp_f32_e32 v90, v90
	v_exp_f32_e32 v91, v91
	v_pk_add_f32 v[120:121], v[120:121], v[84:85]
	v_pk_add_f32 v[122:123], v[122:123], v[86:87]
	s_setprio 2
	s_waitcnt vmcnt(2) lgkmcnt(8)
	s_barrier
	v_mfma_f32_32x32x64_f8f6f4 v[64:79], v[0:5], v[96:101], 0 cbsz:2 blgp:2
	ds_read_b128 v[0:3], v124 offset:36864
	ds_read_b64 v[4:5], v125 offset:40960
	v_exp_f32_e32 v92, v92
	v_exp_f32_e32 v93, v93
	v_exp_f32_e32 v94, v94
	v_exp_f32_e32 v95, v95
	v_pk_add_f32 v[120:121], v[120:121], v[88:89]
	v_pk_add_f32 v[122:123], v[122:123], v[90:91]
	v_mfma_f32_32x32x64_f8f6f4 v[64:79], v[6:11], v[102:107], v[64:79] cbsz:2 blgp:2
	ds_read_b128 v[6:9], v124 offset:37888
	ds_read_b64 v[10:11], v125 offset:41472
	v_exp_f32_e32 v48, v48
	v_exp_f32_e32 v49, v49
	v_exp_f32_e32 v50, v50
	v_exp_f32_e32 v51, v51
	v_pk_add_f32 v[120:121], v[120:121], v[92:93]
	v_pk_add_f32 v[122:123], v[122:123], v[94:95]
	v_mfma_f32_32x32x64_f8f6f4 v[64:79], v[12:17], v[108:113], v[64:79] cbsz:2 blgp:2
	ds_read_b128 v[12:15], v124 offset:38912
	ds_read_b64 v[16:17], v125 offset:41984
	v_exp_f32_e32 v52, v52
	v_exp_f32_e32 v53, v53
	v_exp_f32_e32 v54, v54
	v_exp_f32_e32 v55, v55
	v_pk_add_f32 v[120:121], v[120:121], v[48:49]
	v_pk_add_f32 v[122:123], v[122:123], v[50:51]
	v_mfma_f32_32x32x64_f8f6f4 v[64:79], v[18:23], v[114:119], v[64:79] cbsz:2 blgp:2
	ds_read_b128 v[18:21], v124 offset:39936
	ds_read_b64 v[22:23], v125 offset:42496
	v_exp_f32_e32 v56, v56
	v_exp_f32_e32 v57, v57
	v_exp_f32_e32 v58, v58
	v_exp_f32_e32 v59, v59
	v_pk_add_f32 v[120:121], v[120:121], v[52:53]
	v_pk_add_f32 v[122:123], v[122:123], v[54:55]
	s_waitcnt lgkmcnt(8)
	v_mfma_f32_32x32x64_f8f6f4 v[80:95], v[24:29], v[96:101], 0 cbsz:2 blgp:2
	ds_read_b128 v[24:27], v124 offset:43008
	ds_read_b64 v[28:29], v125 offset:47104
	v_exp_f32_e32 v60, v60
	v_exp_f32_e32 v61, v61
	v_exp_f32_e32 v62, v62
	v_exp_f32_e32 v63, v63
	v_pk_add_f32 v[120:121], v[120:121], v[56:57]
	v_pk_add_f32 v[122:123], v[122:123], v[58:59]
	v_mfma_f32_32x32x64_f8f6f4 v[80:95], v[30:35], v[102:107], v[80:95] cbsz:2 blgp:2
	ds_read_b128 v[30:33], v124 offset:44032
	ds_read_b64 v[34:35], v125 offset:47616
	v_exp_f32_e32 v64, v64
	v_exp_f32_e32 v65, v65
	v_exp_f32_e32 v66, v66
	v_exp_f32_e32 v67, v67
	v_pk_add_f32 v[120:121], v[120:121], v[60:61]
	v_pk_add_f32 v[122:123], v[122:123], v[62:63]
	v_mfma_f32_32x32x64_f8f6f4 v[80:95], v[36:41], v[108:113], v[80:95] cbsz:2 blgp:2
	ds_read_b128 v[36:39], v124 offset:45056
	ds_read_b64 v[40:41], v125 offset:48128
	v_exp_f32_e32 v68, v68
	v_exp_f32_e32 v69, v69
	v_exp_f32_e32 v70, v70
	v_exp_f32_e32 v71, v71
	v_pk_add_f32 v[120:121], v[120:121], v[64:65]
	v_pk_add_f32 v[122:123], v[122:123], v[66:67]
	v_mfma_f32_32x32x64_f8f6f4 v[80:95], v[42:47], v[114:119], v[80:95] cbsz:2 blgp:2
	ds_read_b128 v[42:45], v124 offset:46080
	ds_read_b64 v[46:47], v125 offset:48640
	v_exp_f32_e32 v72, v72
	v_exp_f32_e32 v73, v73
	v_exp_f32_e32 v74, v74
	v_exp_f32_e32 v75, v75
	v_pk_add_f32 v[120:121], v[120:121], v[68:69]
	v_pk_add_f32 v[122:123], v[122:123], v[70:71]
	s_waitcnt vmcnt(1) lgkmcnt(8)
	s_barrier
	v_mfma_f32_32x32x64_f8f6f4 v[48:63], v[0:5], v[96:101], 0 cbsz:2 blgp:2
	ds_read_b128 v[0:3], v124 offset:49152
	ds_read_b64 v[4:5], v125 offset:53248
	v_exp_f32_e32 v76, v76
	v_exp_f32_e32 v77, v77
	v_exp_f32_e32 v78, v78
	v_exp_f32_e32 v79, v79
	v_pk_add_f32 v[120:121], v[120:121], v[72:73]
	v_pk_add_f32 v[122:123], v[122:123], v[74:75]
	v_mfma_f32_32x32x64_f8f6f4 v[48:63], v[6:11], v[102:107], v[48:63] cbsz:2 blgp:2
	ds_read_b128 v[6:9], v124 offset:50176
	ds_read_b64 v[10:11], v125 offset:53760
	v_exp_f32_e32 v80, v80
	v_exp_f32_e32 v81, v81
	v_exp_f32_e32 v82, v82
	v_exp_f32_e32 v83, v83
	v_pk_add_f32 v[120:121], v[120:121], v[76:77]
	v_pk_add_f32 v[122:123], v[122:123], v[78:79]
	v_mfma_f32_32x32x64_f8f6f4 v[48:63], v[12:17], v[108:113], v[48:63] cbsz:2 blgp:2
	ds_read_b128 v[12:15], v124 offset:51200
	ds_read_b64 v[16:17], v125 offset:54272
	v_exp_f32_e32 v84, v84
	v_exp_f32_e32 v85, v85
	v_exp_f32_e32 v86, v86
	v_exp_f32_e32 v87, v87
	v_pk_add_f32 v[120:121], v[120:121], v[80:81]
	v_pk_add_f32 v[122:123], v[122:123], v[82:83]
	v_mfma_f32_32x32x64_f8f6f4 v[48:63], v[18:23], v[114:119], v[48:63] cbsz:2 blgp:2
	ds_read_b128 v[18:21], v124 offset:52224
	ds_read_b64 v[22:23], v125 offset:54784
	v_exp_f32_e32 v88, v88
	v_exp_f32_e32 v89, v89
	v_exp_f32_e32 v90, v90
	v_exp_f32_e32 v91, v91
	v_pk_add_f32 v[120:121], v[120:121], v[84:85]
	v_pk_add_f32 v[122:123], v[122:123], v[86:87]
	s_waitcnt lgkmcnt(8)
	v_mfma_f32_32x32x64_f8f6f4 v[64:79], v[24:29], v[96:101], 0 cbsz:2 blgp:2
	ds_read_b128 v[24:27], v124 offset:55296
	ds_read_b64 v[28:29], v125 offset:59392
	v_exp_f32_e32 v92, v92
	v_exp_f32_e32 v93, v93
	v_exp_f32_e32 v94, v94
	v_exp_f32_e32 v95, v95
	v_pk_add_f32 v[120:121], v[120:121], v[88:89]
	v_pk_add_f32 v[122:123], v[122:123], v[90:91]
	v_mfma_f32_32x32x64_f8f6f4 v[64:79], v[30:35], v[102:107], v[64:79] cbsz:2 blgp:2
	ds_read_b128 v[30:33], v124 offset:56320
	ds_read_b64 v[34:35], v125 offset:59904
	v_exp_f32_e32 v48, v48
	v_exp_f32_e32 v49, v49
	v_exp_f32_e32 v50, v50
	v_exp_f32_e32 v51, v51
	v_pk_add_f32 v[120:121], v[120:121], v[92:93]
	v_pk_add_f32 v[122:123], v[122:123], v[94:95]
	v_mfma_f32_32x32x64_f8f6f4 v[64:79], v[36:41], v[108:113], v[64:79] cbsz:2 blgp:2
	ds_read_b128 v[36:39], v124 offset:57344
	ds_read_b64 v[40:41], v125 offset:60416
	v_exp_f32_e32 v52, v52
	v_exp_f32_e32 v53, v53
	v_exp_f32_e32 v54, v54
	v_exp_f32_e32 v55, v55
	v_pk_add_f32 v[120:121], v[120:121], v[48:49]
	v_pk_add_f32 v[122:123], v[122:123], v[50:51]
	v_mfma_f32_32x32x64_f8f6f4 v[64:79], v[42:47], v[114:119], v[64:79] cbsz:2 blgp:2
	ds_read_b128 v[42:45], v124 offset:58368
	ds_read_b64 v[46:47], v125 offset:60928
	v_exp_f32_e32 v56, v56
	v_exp_f32_e32 v57, v57
	v_exp_f32_e32 v58, v58
	v_exp_f32_e32 v59, v59
	v_pk_add_f32 v[120:121], v[120:121], v[52:53]
	v_pk_add_f32 v[122:123], v[122:123], v[54:55]
	s_setprio 1
	s_waitcnt vmcnt(0) lgkmcnt(8)
	s_barrier
	v_mfma_f32_32x32x64_f8f6f4 v[80:95], v[0:5], v[96:101], 0 cbsz:2 blgp:2
	ds_read_b128 v[0:3], v124
	ds_read_b64 v[4:5], v125 offset:4096
	v_exp_f32_e32 v60, v60
	v_exp_f32_e32 v61, v61
	v_exp_f32_e32 v62, v62
	v_exp_f32_e32 v63, v63
	v_pk_add_f32 v[120:121], v[120:121], v[56:57]
	v_pk_add_f32 v[122:123], v[122:123], v[58:59]
	v_mfma_f32_32x32x64_f8f6f4 v[80:95], v[6:11], v[102:107], v[80:95] cbsz:2 blgp:2
	ds_read_b128 v[6:9], v124 offset:1024
	ds_read_b64 v[10:11], v125 offset:4608
	v_exp_f32_e32 v64, v64
	v_exp_f32_e32 v65, v65
	v_exp_f32_e32 v66, v66
	v_exp_f32_e32 v67, v67
	v_pk_add_f32 v[120:121], v[120:121], v[60:61]
	v_pk_add_f32 v[122:123], v[122:123], v[62:63]
	v_mfma_f32_32x32x64_f8f6f4 v[80:95], v[12:17], v[108:113], v[80:95] cbsz:2 blgp:2
	ds_read_b128 v[12:15], v124 offset:2048
	ds_read_b64 v[16:17], v125 offset:5120
	v_exp_f32_e32 v68, v68
	v_exp_f32_e32 v69, v69
	v_exp_f32_e32 v70, v70
	v_exp_f32_e32 v71, v71
	v_pk_add_f32 v[120:121], v[120:121], v[64:65]
	v_pk_add_f32 v[122:123], v[122:123], v[66:67]
	v_mfma_f32_32x32x64_f8f6f4 v[80:95], v[18:23], v[114:119], v[80:95] cbsz:2 blgp:2
	ds_read_b128 v[18:21], v124 offset:3072
	ds_read_b64 v[22:23], v125 offset:5632
	v_exp_f32_e32 v72, v72
	v_exp_f32_e32 v73, v73
	v_exp_f32_e32 v74, v74
	v_exp_f32_e32 v75, v75
	v_pk_add_f32 v[120:121], v[120:121], v[68:69]
	v_pk_add_f32 v[122:123], v[122:123], v[70:71]
	s_waitcnt lgkmcnt(8)
	v_mfma_f32_32x32x64_f8f6f4 v[48:63], v[24:29], v[96:101], 0 cbsz:2 blgp:2
	ds_read_b128 v[24:27], v124 offset:6144
	ds_read_b64 v[28:29], v125 offset:10240
	v_exp_f32_e32 v76, v76
	v_exp_f32_e32 v77, v77
	v_exp_f32_e32 v78, v78
	v_exp_f32_e32 v79, v79
	v_pk_add_f32 v[120:121], v[120:121], v[72:73]
	v_pk_add_f32 v[122:123], v[122:123], v[74:75]
	v_mfma_f32_32x32x64_f8f6f4 v[48:63], v[30:35], v[102:107], v[48:63] cbsz:2 blgp:2
	ds_read_b128 v[30:33], v124 offset:7168
	ds_read_b64 v[34:35], v125 offset:10752
	v_exp_f32_e32 v80, v80
	v_exp_f32_e32 v81, v81
	v_exp_f32_e32 v82, v82
	v_exp_f32_e32 v83, v83
	v_pk_add_f32 v[120:121], v[120:121], v[76:77]
	v_pk_add_f32 v[122:123], v[122:123], v[78:79]
	s_cmp_lg_u32 s8, 10
	s_cbranch_scc1 .Lmk_nosplit_b
	v_add_f32_e32 v127, v120, v121
	v_add_f32_e32 v126, v122, v123
	v_mov_b32_e32 v120, 0
	v_mov_b32_e32 v121, 0
	v_mov_b32_e32 v122, 0
	v_mov_b32_e32 v123, 0
	v_add_f32_e32 v127, v127, v126
